# compact grid barrier: all workgroups poll the top word (one hop less) at 10 seams, plus XCD-local barriers at 4 seams, runtime placement check
# speedup vs baseline: 1.0298x; 1.0124x over previous
; __device__ __forceinline__ u64_t* ssq_ptr(unsigned char* ws, int v) { return (u64_t*)(ws + CTL_SSQ) + (size_t)v * NTOK; }
; #define OPAQUE_WS() unsigned char* ws = P.ws; asm volatile("" : "+s"(ws)); F.ws = ws; F.tid = fresh_tid(F.wave); asm volatile("" : "+v"(F.tid)); F.lane = F.tid & 63; int c = F.bid; asm volatile("" : "+s"(c))
; #define REP_BEGIN(k) for (int rep_ = 0, nrep_ = ((k) >= PROBE_LO && (k) < PROBE_HI) ? PROBE_N : 0; rep_ <= nrep_; ++rep_) { const bool rerun = PROBE_AFTER ? (rep_ > 0) : (rep_ < nrep_), dry = rerun && PROBE_DRY_;
; __global__ void __launch_bounds__(NTHREADS, 2) mk_fwd(Params P) {
;     ...
; #pragma unroll 1
;     for (int l = 0; l < DEPTH; ++l) {
;         const int pb = 1 + 9 * l;
;         if (PH_EN(0) && IN(pb + 0)) { REP_BEGIN(pb + 0) OPAQUE_WS(); int lq = l; asm volatile("" : "+s"(lq));
;             if (lq == 0 && !rerun) { phase_dense_w13_b(F, P); xcd_barrier(bar); }
;             if (lq > 0) {
;                 { const int gw = F.bid * NWAVES + F.wave, NGW = F.G * NWAVES; const u64_t* ssq = ssq_ptr(ws, 3 * lq); float* rsq = (float*)(ws + WS_RSQA);
;                   quant_pass((const bf16_t*)(ws + WS_XB), ws + AR_XQA, rsq, ssq, gw, NGW, F.lane, dry); }
;                 xcd_barrier(bar);
;             }
;             { Sched2D Sg{(const char*)(ws + AR_XQA), (const char*)(ws + WB_WIN + lq * SZ_WIN), NTOK / 256, OFF_GL / 256, D / 2, G, c, 0, (NTOK / 256) * (OFF_GL / 256)};
;               EpiIn E{ws, P, lq, dry, rerun};
;               pg8::gemm_phase<EpiIn, Sched2D, true, true, true>(F.lds, D / 2, Sg, E, F.wave); }
.LBB0_223:
	s_or_b64 exec, exec, s[30:31]
	v_readlane_b32 s100, v253, 53
	v_readlane_b32 s101, v253, 54
	v_mov_b32_e32 v8, 0
	s_nop 4
	global_load_dwordx4 v[0:3], v8, s[100:101] offset:64 sc1
	global_load_dwordx4 v[4:7], v8, s[100:101] offset:80 sc1
	s_waitcnt vmcnt(0)
	v_bcnt_u32_b32 v8, v0, 0
	v_bcnt_u32_b32 v8, v1, v8
	v_bcnt_u32_b32 v8, v2, v8
	v_bcnt_u32_b32 v8, v3, v8
	v_bcnt_u32_b32 v8, v4, v8
	v_bcnt_u32_b32 v8, v5, v8
	v_bcnt_u32_b32 v8, v6, v8
	v_bcnt_u32_b32 v8, v7, v8
	v_or3_b32 v9, v0, v1, v2
	v_or3_b32 v9, v9, v3, v4
	v_or3_b32 v9, v9, v5, v6
	v_or_b32_e32 v9, v9, v7
	v_bcnt_u32_b32 v9, v9, 0
	v_min_u32_e32 v0, v0, v1
	v_min_u32_e32 v2, v2, v3
	v_min_u32_e32 v4, v4, v5
	v_min_u32_e32 v6, v6, v7
	v_min3_u32 v0, v0, v2, v4
	v_min_u32_e32 v0, v0, v6
	v_readfirstlane_b32 s100, v8
	v_readfirstlane_b32 s101, v0
	s_cmp_eq_u32 s100, 8
	s_cselect_b32 s100, 1, 0
	s_cmp_lg_u32 s101, 0
	s_cselect_b32 s100, s100, 0
	v_readfirstlane_b32 s101, v9
	s_cmp_eq_u32 s101, 8
	s_cselect_b32 s100, s100, 0
	s_cmpk_eq_i32 s78, 0x100
	s_cselect_b32 s100, s100, 0
	s_lshl_b32 s0, s38, 14
	s_add_i32 s0, s0, 0
	s_cmpk_lt_i32 s96, 0xe00
	v_writelane_b32 v254, s0, 28
	s_cselect_b64 s[0:1], -1, 0
	v_writelane_b32 v254, s0, 29
	s_cmpk_lt_i32 s96, 0x700
	s_mov_b32 s93, 0
	v_writelane_b32 v254, s1, 30
	s_cselect_b64 s[0:1], -1, 0
	v_writelane_b32 v254, s0, 31
	s_cmpk_lt_i32 s96, 0x1700
	s_movk_i32 s84, 0x4000
	v_writelane_b32 v254, s1, 32
	s_cselect_b64 s[0:1], -1, 0
	v_writelane_b32 v254, s0, 33
	s_lshl_b32 s2, s78, 5
	s_ashr_i32 s95, s78, 31
	v_writelane_b32 v254, s1, 34
	s_bfe_u32 s0, s33, 0x20006
	v_writelane_b32 v254, s0, 19
	s_lshl_b32 s0, s0, 7
	s_cmpk_lt_i32 s96, 0x4000
	v_writelane_b32 v254, s0, 35
	s_cselect_b64 s[0:1], -1, 0
	s_cmpk_eq_i32 s78, 0x100
	s_cselect_b64 s[4:5], -1, 0
	v_writelane_b32 v254, s4, 10
	v_mov_b32_e32 v113, 0
	v_mov_b32_e32 v248, 1
	v_writelane_b32 v254, s5, 11
	s_add_u32 s4, s86, 0x1000
	s_addc_u32 s5, s87, 0
	v_writelane_b32 v254, s4, 36
	s_cmpk_lt_i32 s96, 0x1c00
	s_mov_b32 s86, s2
	v_writelane_b32 v254, s5, 37
	s_cselect_b64 s[2:3], -1, 0
	v_writelane_b32 v254, s2, 38
	s_cmp_lt_i32 s96, 0xa800
	v_readlane_b32 s4, v253, 0
	v_writelane_b32 v254, s3, 39
	s_cselect_b64 s[2:3], -1, 0
	v_writelane_b32 v254, s2, 40
	s_ashr_i32 s97, s96, 31
	s_ashr_i32 s87, s86, 31
	v_writelane_b32 v254, s3, 41
	s_lshl_b32 s2, s4, 8
	s_lshl_b32 s3, s38, 5
	s_add_i32 s5, s2, s3
	s_lshl_b32 s2, s4, 7
	s_lshl_b32 s3, s38, 4
	s_add_i32 s6, s2, s3
	s_lshl_b32 s2, s4, 4
	s_lshl_b32 s3, s38, 1
	s_add_i32 s7, s2, s3
	s_lshl_b32 s2, s4, 10
	s_lshl_b32 s3, s38, 7
	s_add_i32 s2, s2, s3
	v_writelane_b32 v254, s2, 42
	s_lshl_b32 s2, s4, 11
	s_lshl_b32 s3, s38, 8
	s_add_i32 s2, s2, s3
	v_writelane_b32 v254, s2, 43
	v_writelane_b32 v254, s5, 44
	s_or_b32 s2, s5, 3
	v_writelane_b32 v254, s2, 45
	s_or_b32 s2, s6, 3
	v_writelane_b32 v254, s2, 46
	s_or_b32 s2, s6, 2
	v_writelane_b32 v254, s2, 47
	v_writelane_b32 v254, s6, 48
	s_or_b32 s2, s6, 1
	v_writelane_b32 v254, s2, 49
	s_lshl_b32 s2, s4, 6
	s_lshl_b32 s3, s38, 3
	s_add_i32 s2, s2, s3
	s_add_i32 s2, s2, 0x7ffff200
	v_writelane_b32 v254, s2, 50
	s_lshl_b32 s2, s78, 6
	v_writelane_b32 v254, s2, 51
	s_lshl_b32 s2, s38, 6
	s_add_i32 s2, s36, s2
	v_writelane_b32 v254, s2, 52
	s_sub_i32 s2, 0xa7ff, s96
	s_lshl_b32 s3, s2, 5
	v_writelane_b32 v254, s3, 53
	v_writelane_b32 v254, s2, 54
	s_lshl_b32 s2, s2, 1
	v_writelane_b32 v254, s2, 55
	v_writelane_b32 v254, s7, 56
	s_or_b32 s2, s7, 1
	v_writelane_b32 v254, s2, 57
	s_lshl_b64 s[2:3], s[96:97], 12
	v_writelane_b32 v254, s2, 58
	s_lshl_b32 s75, s78, 8
	s_lshl_b32 s79, s78, 7
	v_writelane_b32 v254, s3, 59
	s_lshl_b64 s[2:3], s[86:87], 12
	v_writelane_b32 v254, s2, 60
	s_lshl_b32 s81, s78, 4
	s_lshl_b32 s82, s78, 10
	s_lshl_b32 s89, s78, 11
	v_writelane_b32 v254, s3, 61
	s_lshl_b64 s[2:3], s[96:97], 11
	s_add_u32 s2, s2, 0x4f00400
	v_writelane_b32 v254, s2, 62
	s_addc_u32 s2, s3, 0
	v_writelane_b32 v254, s2, 63
	s_mov_b32 s2, s96
	v_writelane_b32 v255, s2, 0
	s_xor_b64 s[0:1], s[0:1], -1
	s_movk_i32 s97, 0xe00
	v_writelane_b32 v255, s3, 1
	s_add_i32 s2, s96, s76
	s_ashr_i32 s3, s2, 31
	s_lshl_b64 s[2:3], s[2:3], 12
	v_writelane_b32 v255, s2, 2
	s_movk_i32 s96, 0x5c00
	s_mov_b32 s73, 0x8000
	v_writelane_b32 v255, s3, 3
	s_add_i32 s2, 0, 0x23fa0
	v_writelane_b32 v254, s2, 8
	s_add_i32 s2, 0, 0x23fa4
	v_writelane_b32 v255, s0, 4
	v_writelane_b32 v254, s2, 9
	v_mov_b32_e32 v249, 0x358637bd
	v_writelane_b32 v255, s1, 5
	s_add_i32 s0, 0, 0x11000
	v_writelane_b32 v254, s0, 13
	s_add_i32 s0, 0, 0x1115c
	v_writelane_b32 v254, s0, 12
	s_add_i32 s0, 0, 0x23fc0
	v_writelane_b32 v254, s0, 15
	s_add_i32 s0, 0, 0x23fd0
	v_writelane_b32 v254, s0, 16
	s_add_i32 s0, 0, 0x23fdc
	v_writelane_b32 v255, s0, 6
	s_lshl_b64 s[0:1], s[86:87], 11
	v_writelane_b32 v255, s0, 7
	s_mov_b32 s92, 0xa000
	v_mov_b32_e32 v250, 0x1000
	v_writelane_b32 v255, s1, 8
	s_mov_b32 s0, s76
	v_writelane_b32 v255, s0, 9
	v_mbcnt_hi_u32_b32 v251, -1, v82
	v_mov_b32_e32 v252, 0xf149f2ca
	v_writelane_b32 v255, s1, 10
	s_mov_b32 s0, s86
	v_writelane_b32 v255, s0, 11
	v_mov_b32_e32 v164, 0x43e00000
	s_movk_i32 s85, 0x80
	v_writelane_b32 v255, s1, 12
	v_writelane_b32 v255, s75, 13
	v_writelane_b32 v255, s79, 14
	v_writelane_b32 v255, s81, 15
	v_writelane_b32 v255, s82, 16
	s_mov_b32 s60, 0xc000
	s_mov_b32 s61, 0xe000
	s_mov_b32 s80, 0x41000000
	s_mov_b32 s70, 0xc3e00000
	s_mov_b64 s[34:35], -1
	s_mov_b64 s[66:67], 0x2000
	s_mov_b32 s36, s93
	v_writelane_b32 v254, s95, 14
	v_writelane_b32 v255, s89, 17
	s_waitcnt lgkmcnt(0)
	s_barrier
	s_branch .LBB0_227

; __device__ __forceinline__ int fresh_tid(int wave) { return wave * 64 + fresh_lane(); }
; __device__ __forceinline__ unsigned xb_ld(unsigned* p)              { return __hip_atomic_load(p, __ATOMIC_RELAXED, __HIP_MEMORY_SCOPE_AGENT); }
; __device__ __forceinline__ unsigned xb_add(unsigned* p, unsigned v) { return __hip_atomic_fetch_add(p, v, __ATOMIC_RELAXED, __HIP_MEMORY_SCOPE_AGENT); }
; __device__ __forceinline__ unsigned xb_xcc_id() { return (unsigned)__builtin_amdgcn_s_getreg((3 << 11) | 20) & 0xFu; }
; #define XB_SPIN(cond, bar) do { unsigned _sp = 0; while (cond) { __builtin_amdgcn_s_sleep(1); \
;     if ((++_sp & 255u) == 0u) { if (xb_ld(&(bar)[XB_TMO])) break; if (_sp > XB_SPIN_CAP) { atomicAdd(&(bar)[XB_TMO], 1u); break; } } } } while (0)
; __device__ __forceinline__ void xcd_barrier(const XcdBarrier& b) {
;     ...
;     if (fresh_tid(b.wave) == 0) {
;         unsigned* bar = b.bar; asm volatile("" : "+s"(bar));
;         __builtin_amdgcn_s_waitcnt(0);
;         const unsigned bx = xb_xcc_id();
;         unsigned nloc = b.st[0], nx = b.st[1];
;         if (nloc == 0u) { xcd_barrier_complete(bar, bx, nloc, nx); b.st[0] = nloc; b.st[1] = nx; }
;         const unsigned old = xb_add(&bar[XB_XSUB(bx)], 1u);
;         const unsigned gen = old / nloc;
;         if (old + 1u == (gen + 1u) * nloc) {
;             __builtin_amdgcn_fence(__ATOMIC_RELEASE, "agent");
;             asm volatile("s_waitcnt vmcnt(0)" ::: "memory");
;             const unsigned og = xb_add(&bar[XB_TOP], 1u);
;             const unsigned tg = og / nx;
;             if (og + 1u == (tg + 1u) * nx) xb_add(&bar[XB_TOPGEN], 1u);
;             else XB_SPIN(xb_ld(&bar[XB_TOPGEN]) == tg, bar);
;             __builtin_amdgcn_fence(__ATOMIC_ACQUIRE, "agent");
;             xb_add(&bar[XB_XGEN(bx)], 1u);
;             asm volatile("s_waitcnt vmcnt(0)" ::: "memory");
;         } else {
;             XB_SPIN(xb_ld(&bar[XB_XGEN(bx)]) == gen, bar);
;             __builtin_amdgcn_fence(__ATOMIC_ACQUIRE, "agent");
;             asm volatile("s_waitcnt vmcnt(0)" ::: "memory");
;         }
.LBB0_237:
	s_mov_b32 s0, s93
	s_waitcnt lgkmcnt(0)
	s_barrier
	s_waitcnt vmcnt(0)
	s_barrier
	s_nop 0
	v_mbcnt_lo_u32_b32 v0, -1, s0
	v_mbcnt_hi_u32_b32 v0, -1, v0
	v_readlane_b32 s0, v254, 17
	s_nop 1
	v_cmp_eq_u32_e32 vcc, s0, v0
	s_and_saveexec_b64 s[30:31], vcc
	s_mov_b32 s73, 0x8000
	s_mov_b32 s92, 0xa000
	s_cbranch_execz .LBB0_281
	s_bitcmp1_b32 s100, 0
	s_cbranch_scc0 .Lgb0_orig
	v_readlane_b32 s40, v253, 53
	v_readlane_b32 s41, v253, 54
	s_getreg_b32 s0, hwreg(HW_REG_XCC_ID, 0, 4)
	v_mov_b32_e32 v1, 1
	s_and_b32 s0, s0, 15
	s_lshl_b32 s0, s0, 8
	s_addk_i32 s0, 0x1400
	v_mov_b32_e32 v0, s0
	s_waitcnt vmcnt(0) lgkmcnt(0)
	global_atomic_add v2, v0, v1, s[40:41] sc0
	s_waitcnt vmcnt(0)
	v_readfirstlane_b32 s0, v2
	s_lshr_b32 s1, s0, 5
	s_and_b32 s0, s0, 31
	s_add_i32 s1, s1, 1
	s_lshl_b32 s1, s1, 3
	s_cmp_lg_u32 s0, 31
	s_cbranch_scc1 .Lgb0_poll
	buffer_wbl2 sc1
	s_waitcnt vmcnt(0)
	v_add_u32_e32 v0, 0x1000, v0
	global_atomic_add v0, v1, s[40:41]
	v_mov_b32_e32 v0, 0x3400
	global_atomic_add v2, v0, v1, s[40:41] sc0
	s_waitcnt vmcnt(0)
	v_readfirstlane_b32 s0, v2
	s_add_i32 s0, s0, 1
	s_cmp_lg_u32 s0, s1
	s_cbranch_scc1 .Lgb0_poll
	v_mov_b32_e32 v0, 0x3500
	global_atomic_add v0, v1, s[40:41]
	s_branch .Lgb0_done
.Lgb0_poll:
	v_mov_b32_e32 v0, 0x3400
	s_mov_b32 s0, 0
.Lgb0_spin:
	global_load_dword v3, v0, s[40:41] sc1
	s_waitcnt vmcnt(0)
	v_subrev_u32_e32 v3, s1, v3
	v_cmp_gt_i32_e32 vcc, 0, v3
	s_cbranch_vccz .Lgb0_done
	s_sleep 1
	s_add_i32 s0, s0, 1
	s_cmp_lt_u32 s0, 0x100000
	s_cbranch_scc1 .Lgb0_spin

; __device__ __forceinline__ int fresh_tid(int wave) { return wave * 64 + fresh_lane(); }
; __device__ __forceinline__ unsigned xb_ld(unsigned* p)              { return __hip_atomic_load(p, __ATOMIC_RELAXED, __HIP_MEMORY_SCOPE_AGENT); }
; __device__ __forceinline__ unsigned xb_xcc_id() { return (unsigned)__builtin_amdgcn_s_getreg((3 << 11) | 20) & 0xFu; }
; __device__ __forceinline__ void xcd_barrier_complete(unsigned* bar, unsigned x, unsigned& nloc, unsigned& nx) {
;     const unsigned G = gridDim.x * gridDim.y * gridDim.z;
;     unsigned sum, cnt, mine, sp = 0u;
;     for (;;) {
;         sum = 0u; cnt = 0u; mine = 0u;
; #pragma unroll
;         for (unsigned j = 0; j < 16; ++j) { const unsigned c = xb_ld(&bar[XB_XCNT(j)]); sum += c; cnt += (c > 0u) ? 1u : 0u; mine = (j == x) ? c : mine; }
;         if (sum == G) break;
;         __builtin_amdgcn_s_sleep(1);
;         if ((++sp & 255u) == 0u) { if (xb_ld(&bar[XB_TMO])) break; if (sp > XB_SPIN_CAP) { atomicAdd(&bar[XB_TMO], 1u); break; } }
;     }
;     nloc = mine > 0u ? mine : 1u; nx = cnt > 0u ? cnt : 1u;
; }
; __device__ __forceinline__ void xcd_barrier(const XcdBarrier& b) {
;     ...
;     if (fresh_tid(b.wave) == 0) {
;         unsigned* bar = b.bar; asm volatile("" : "+s"(bar));
;         __builtin_amdgcn_s_waitcnt(0);
;         const unsigned bx = xb_xcc_id();
;         unsigned nloc = b.st[0], nx = b.st[1];
;         if (nloc == 0u) { xcd_barrier_complete(bar, bx, nloc, nx); b.st[0] = nloc; b.st[1] = nx; }
.Lgb0_orig:
	v_readlane_b32 s40, v253, 53
	v_readlane_b32 s1, v254, 8
	v_readlane_b32 s41, v253, 54
	s_waitcnt vmcnt(0) expcnt(0) lgkmcnt(0)
	v_mov_b32_e32 v0, s1
	s_getreg_b32 s0, hwreg(HW_REG_XCC_ID, 0, 4)
	ds_read_b32 v2, v0
	v_readlane_b32 s1, v254, 9
	s_and_b32 s42, s0, 15
	s_waitcnt lgkmcnt(0)
	v_cmp_ne_u32_e32 vcc, 0, v2
	v_mov_b32_e32 v0, s1
	ds_read_b32 v0, v0
	s_cbranch_vccnz .LBB0_252
	v_readlane_b32 s0, v253, 3
	v_readlane_b32 s1, v253, 4
	s_load_dwordx2 s[4:5], s[0:1], 0x4
	s_add_u32 s0, s40, 0x1000
	s_addc_u32 s1, s41, 0
	s_add_u32 s2, s40, 0x1100
	s_addc_u32 s3, s41, 0
	s_waitcnt lgkmcnt(0)
	s_mul_i32 s26, s4, s78
	s_add_u32 s4, s40, 0x1200
	s_mul_i32 s26, s26, s5
	s_addc_u32 s5, s41, 0
	s_add_u32 s6, s40, 0x1300
	s_addc_u32 s7, s41, 0
	s_mov_b32 s27, 1
	s_mov_b64 s[8:9], 0
	s_branch .LBB0_242

; __device__ __forceinline__ int fresh_tid(int wave) { return wave * 64 + fresh_lane(); }
; __device__ __forceinline__ unsigned xb_ld(unsigned* p)              { return __hip_atomic_load(p, __ATOMIC_RELAXED, __HIP_MEMORY_SCOPE_AGENT); }
; __device__ __forceinline__ unsigned xb_add(unsigned* p, unsigned v) { return __hip_atomic_fetch_add(p, v, __ATOMIC_RELAXED, __HIP_MEMORY_SCOPE_AGENT); }
; __device__ __forceinline__ unsigned xb_xcc_id() { return (unsigned)__builtin_amdgcn_s_getreg((3 << 11) | 20) & 0xFu; }
; #define XB_SPIN(cond, bar) do { unsigned _sp = 0; while (cond) { __builtin_amdgcn_s_sleep(1); \
;     if ((++_sp & 255u) == 0u) { if (xb_ld(&(bar)[XB_TMO])) break; if (_sp > XB_SPIN_CAP) { atomicAdd(&(bar)[XB_TMO], 1u); break; } } } } while (0)
; __device__ __forceinline__ void xcd_barrier(const XcdBarrier& b) {
;     ...
;     if (fresh_tid(b.wave) == 0) {
;         unsigned* bar = b.bar; asm volatile("" : "+s"(bar));
;         __builtin_amdgcn_s_waitcnt(0);
;         const unsigned bx = xb_xcc_id();
;         unsigned nloc = b.st[0], nx = b.st[1];
;         if (nloc == 0u) { xcd_barrier_complete(bar, bx, nloc, nx); b.st[0] = nloc; b.st[1] = nx; }
;         const unsigned old = xb_add(&bar[XB_XSUB(bx)], 1u);
;         const unsigned gen = old / nloc;
;         if (old + 1u == (gen + 1u) * nloc) {
;             __builtin_amdgcn_fence(__ATOMIC_RELEASE, "agent");
;             asm volatile("s_waitcnt vmcnt(0)" ::: "memory");
;             const unsigned og = xb_add(&bar[XB_TOP], 1u);
;             const unsigned tg = og / nx;
;             if (og + 1u == (tg + 1u) * nx) xb_add(&bar[XB_TOPGEN], 1u);
;             else XB_SPIN(xb_ld(&bar[XB_TOPGEN]) == tg, bar);
;             __builtin_amdgcn_fence(__ATOMIC_ACQUIRE, "agent");
;             xb_add(&bar[XB_XGEN(bx)], 1u);
;             asm volatile("s_waitcnt vmcnt(0)" ::: "memory");
;         } else {
;             XB_SPIN(xb_ld(&bar[XB_XGEN(bx)]) == gen, bar);
;             __builtin_amdgcn_fence(__ATOMIC_ACQUIRE, "agent");
;             asm volatile("s_waitcnt vmcnt(0)" ::: "memory");
;         }
.LBB0_300:
	s_mov_b32 s0, s93
	s_waitcnt vmcnt(0)
	s_waitcnt lgkmcnt(0)
	s_barrier
	s_waitcnt vmcnt(0)
	v_mbcnt_lo_u32_b32 v0, -1, s0
	v_mbcnt_hi_u32_b32 v0, -1, v0
	v_readlane_b32 s0, v254, 17
	s_nop 1
	v_cmp_eq_u32_e32 vcc, s0, v0
	s_and_saveexec_b64 s[0:1], vcc
	s_cbranch_execz .LBB0_344
	s_bitcmp1_b32 s100, 0
	s_cbranch_scc0 .Lgb1_orig
	v_readlane_b32 s40, v253, 53
	v_readlane_b32 s41, v253, 54
	s_getreg_b32 s2, hwreg(HW_REG_XCC_ID, 0, 4)
	v_mov_b32_e32 v1, 1
	s_and_b32 s2, s2, 15
	s_lshl_b32 s2, s2, 8
	s_addk_i32 s2, 0x1400
	v_mov_b32_e32 v0, s2
	s_waitcnt vmcnt(0) lgkmcnt(0)
	global_atomic_add v2, v0, v1, s[40:41] sc0
	s_waitcnt vmcnt(0)
	v_readfirstlane_b32 s2, v2
	s_lshr_b32 s3, s2, 5
	s_and_b32 s2, s2, 31
	s_add_i32 s3, s3, 1
	s_lshl_b32 s3, s3, 3
	s_cmp_lg_u32 s2, 31
	s_cbranch_scc1 .Lgb1_poll
	buffer_wbl2 sc1
	s_waitcnt vmcnt(0)
	v_add_u32_e32 v0, 0x1000, v0
	global_atomic_add v0, v1, s[40:41]
	v_mov_b32_e32 v0, 0x3400
	global_atomic_add v2, v0, v1, s[40:41] sc0
	s_waitcnt vmcnt(0)
	v_readfirstlane_b32 s2, v2
	s_add_i32 s2, s2, 1
	s_cmp_lg_u32 s2, s3
	s_cbranch_scc1 .Lgb1_poll
	v_mov_b32_e32 v0, 0x3500
	global_atomic_add v0, v1, s[40:41]
	s_branch .Lgb1_done
.Lgb1_poll:
	v_mov_b32_e32 v0, 0x3400
	s_mov_b32 s2, 0
.Lgb1_spin:
	global_load_dword v3, v0, s[40:41] sc1
	s_waitcnt vmcnt(0)
	v_subrev_u32_e32 v3, s3, v3
	v_cmp_gt_i32_e32 vcc, 0, v3
	s_cbranch_vccz .Lgb1_done
	s_sleep 1
	s_add_i32 s2, s2, 1
	s_cmp_lt_u32 s2, 0x100000
	s_cbranch_scc1 .Lgb1_spin

; __device__ __forceinline__ int fresh_tid(int wave) { return wave * 64 + fresh_lane(); }
; __device__ __forceinline__ unsigned xb_ld(unsigned* p)              { return __hip_atomic_load(p, __ATOMIC_RELAXED, __HIP_MEMORY_SCOPE_AGENT); }
; __device__ __forceinline__ unsigned xb_xcc_id() { return (unsigned)__builtin_amdgcn_s_getreg((3 << 11) | 20) & 0xFu; }
; __device__ __forceinline__ void xcd_barrier_complete(unsigned* bar, unsigned x, unsigned& nloc, unsigned& nx) {
;     const unsigned G = gridDim.x * gridDim.y * gridDim.z;
;     unsigned sum, cnt, mine, sp = 0u;
;     for (;;) {
;         sum = 0u; cnt = 0u; mine = 0u;
; #pragma unroll
;         for (unsigned j = 0; j < 16; ++j) { const unsigned c = xb_ld(&bar[XB_XCNT(j)]); sum += c; cnt += (c > 0u) ? 1u : 0u; mine = (j == x) ? c : mine; }
;         if (sum == G) break;
;         __builtin_amdgcn_s_sleep(1);
;         if ((++sp & 255u) == 0u) { if (xb_ld(&bar[XB_TMO])) break; if (sp > XB_SPIN_CAP) { atomicAdd(&bar[XB_TMO], 1u); break; } }
;     }
;     nloc = mine > 0u ? mine : 1u; nx = cnt > 0u ? cnt : 1u;
; }
; __device__ __forceinline__ void xcd_barrier(const XcdBarrier& b) {
;     ...
;     if (fresh_tid(b.wave) == 0) {
;         unsigned* bar = b.bar; asm volatile("" : "+s"(bar));
;         __builtin_amdgcn_s_waitcnt(0);
;         const unsigned bx = xb_xcc_id();
;         unsigned nloc = b.st[0], nx = b.st[1];
;         if (nloc == 0u) { xcd_barrier_complete(bar, bx, nloc, nx); b.st[0] = nloc; b.st[1] = nx; }
.Lgb1_orig:
	v_readlane_b32 s40, v253, 53
	v_readlane_b32 s3, v254, 8
	v_readlane_b32 s41, v253, 54
	s_waitcnt vmcnt(0) expcnt(0) lgkmcnt(0)
	v_mov_b32_e32 v0, s3
	s_getreg_b32 s2, hwreg(HW_REG_XCC_ID, 0, 4)
	ds_read_b32 v2, v0
	v_readlane_b32 s3, v254, 9
	s_and_b32 s42, s2, 15
	s_waitcnt lgkmcnt(0)
	v_cmp_ne_u32_e32 vcc, 0, v2
	v_mov_b32_e32 v0, s3
	ds_read_b32 v0, v0
	s_cbranch_vccnz .LBB0_315
	v_readlane_b32 s2, v253, 3
	v_readlane_b32 s3, v253, 4
	s_load_dwordx2 s[6:7], s[2:3], 0x4
	s_add_u32 s2, s40, 0x1000
	s_addc_u32 s3, s41, 0
	s_add_u32 s4, s40, 0x1100
	s_addc_u32 s5, s41, 0
	s_waitcnt lgkmcnt(0)
	s_mul_i32 s28, s6, s78
	s_add_u32 s6, s40, 0x1200
	s_mul_i32 s28, s28, s7
	s_addc_u32 s7, s41, 0
	s_add_u32 s8, s40, 0x1300
	s_addc_u32 s9, s41, 0
	s_mov_b32 s29, 1
	s_mov_b64 s[10:11], 0
	s_branch .LBB0_305

; __device__ __forceinline__ int fresh_tid(int wave) { return wave * 64 + fresh_lane(); }
; __device__ __forceinline__ unsigned xb_ld(unsigned* p)              { return __hip_atomic_load(p, __ATOMIC_RELAXED, __HIP_MEMORY_SCOPE_AGENT); }
; __device__ __forceinline__ unsigned xb_add(unsigned* p, unsigned v) { return __hip_atomic_fetch_add(p, v, __ATOMIC_RELAXED, __HIP_MEMORY_SCOPE_AGENT); }
; __device__ __forceinline__ unsigned xb_xcc_id() { return (unsigned)__builtin_amdgcn_s_getreg((3 << 11) | 20) & 0xFu; }
; #define XB_SPIN(cond, bar) do { unsigned _sp = 0; while (cond) { __builtin_amdgcn_s_sleep(1); \
;     if ((++_sp & 255u) == 0u) { if (xb_ld(&(bar)[XB_TMO])) break; if (_sp > XB_SPIN_CAP) { atomicAdd(&(bar)[XB_TMO], 1u); break; } } } } while (0)
; __device__ __forceinline__ void xcd_barrier(const XcdBarrier& b) {
;     ...
;     if (fresh_tid(b.wave) == 0) {
;         unsigned* bar = b.bar; asm volatile("" : "+s"(bar));
;         __builtin_amdgcn_s_waitcnt(0);
;         const unsigned bx = xb_xcc_id();
;         unsigned nloc = b.st[0], nx = b.st[1];
;         if (nloc == 0u) { xcd_barrier_complete(bar, bx, nloc, nx); b.st[0] = nloc; b.st[1] = nx; }
;         const unsigned old = xb_add(&bar[XB_XSUB(bx)], 1u);
;         const unsigned gen = old / nloc;
;         if (old + 1u == (gen + 1u) * nloc) {
;             __builtin_amdgcn_fence(__ATOMIC_RELEASE, "agent");
;             asm volatile("s_waitcnt vmcnt(0)" ::: "memory");
;             const unsigned og = xb_add(&bar[XB_TOP], 1u);
;             const unsigned tg = og / nx;
;             if (og + 1u == (tg + 1u) * nx) xb_add(&bar[XB_TOPGEN], 1u);
;             else XB_SPIN(xb_ld(&bar[XB_TOPGEN]) == tg, bar);
;             __builtin_amdgcn_fence(__ATOMIC_ACQUIRE, "agent");
;             xb_add(&bar[XB_XGEN(bx)], 1u);
;             asm volatile("s_waitcnt vmcnt(0)" ::: "memory");
;         } else {
;             XB_SPIN(xb_ld(&bar[XB_XGEN(bx)]) == gen, bar);
;             __builtin_amdgcn_fence(__ATOMIC_ACQUIRE, "agent");
;             asm volatile("s_waitcnt vmcnt(0)" ::: "memory");
;         }
.LBB0_462:
	s_mov_b32 s0, s93
	s_waitcnt vmcnt(0)
	s_waitcnt lgkmcnt(0)
	s_barrier
	s_nop 0
	v_mbcnt_lo_u32_b32 v0, -1, s0
	v_mbcnt_hi_u32_b32 v0, -1, v0
	v_readlane_b32 s0, v254, 17
	s_nop 1
	v_cmp_eq_u32_e32 vcc, s0, v0
	s_and_saveexec_b64 s[0:1], vcc
	s_cbranch_execz .LBB0_506
	s_bitcmp1_b32 s100, 0
	s_cbranch_scc0 .Lgb2_orig
	v_readlane_b32 s36, v253, 53
	v_readlane_b32 s37, v253, 54
	s_getreg_b32 s2, hwreg(HW_REG_XCC_ID, 0, 4)
	v_mov_b32_e32 v1, 1
	s_and_b32 s2, s2, 15
	s_lshl_b32 s2, s2, 8
	s_addk_i32 s2, 0x1400
	v_mov_b32_e32 v0, s2
	s_waitcnt vmcnt(0) lgkmcnt(0)
	global_atomic_add v2, v0, v1, s[36:37] sc0
	s_waitcnt vmcnt(0)
	v_readfirstlane_b32 s2, v2
	s_lshr_b32 s3, s2, 5
	s_and_b32 s2, s2, 31
	s_add_i32 s3, s3, 1
	s_lshl_b32 s3, s3, 3
	s_cmp_lg_u32 s2, 31
	s_cbranch_scc1 .Lgb2_poll
	buffer_wbl2 sc1
	s_waitcnt vmcnt(0)
	v_add_u32_e32 v0, 0x1000, v0
	global_atomic_add v0, v1, s[36:37]
	v_mov_b32_e32 v0, 0x3400
	global_atomic_add v2, v0, v1, s[36:37] sc0
	s_waitcnt vmcnt(0)
	v_readfirstlane_b32 s2, v2
	s_add_i32 s2, s2, 1
	s_cmp_lg_u32 s2, s3
	s_cbranch_scc1 .Lgb2_poll
	v_mov_b32_e32 v0, 0x3500
	global_atomic_add v0, v1, s[36:37]
	s_branch .Lgb2_done

; __device__ __forceinline__ unsigned xb_ld(unsigned* p)              { return __hip_atomic_load(p, __ATOMIC_RELAXED, __HIP_MEMORY_SCOPE_AGENT); }
; __device__ __forceinline__ unsigned xb_add(unsigned* p, unsigned v) { return __hip_atomic_fetch_add(p, v, __ATOMIC_RELAXED, __HIP_MEMORY_SCOPE_AGENT); }
; #define XB_SPIN(cond, bar) do { unsigned _sp = 0; while (cond) { __builtin_amdgcn_s_sleep(1); \
;     if ((++_sp & 255u) == 0u) { if (xb_ld(&(bar)[XB_TMO])) break; if (_sp > XB_SPIN_CAP) { atomicAdd(&(bar)[XB_TMO], 1u); break; } } } } while (0)
; __device__ __forceinline__ void xcd_barrier(const XcdBarrier& b) {
;     ...
;             else XB_SPIN(xb_ld(&bar[XB_TOPGEN]) == tg, bar);
;             __builtin_amdgcn_fence(__ATOMIC_ACQUIRE, "agent");
;             xb_add(&bar[XB_XGEN(bx)], 1u);
;             asm volatile("s_waitcnt vmcnt(0)" ::: "memory");
;         } else {
;             XB_SPIN(xb_ld(&bar[XB_XGEN(bx)]) == gen, bar);
.Lgb2_spin:
	global_load_dword v3, v0, s[36:37] sc1
	s_waitcnt vmcnt(0)
	v_subrev_u32_e32 v3, s3, v3
	v_cmp_gt_i32_e32 vcc, 0, v3
	s_cbranch_vccz .Lgb2_done
	s_sleep 1
	s_add_i32 s2, s2, 1
	s_cmp_lt_u32 s2, 0x100000
	s_cbranch_scc1 .Lgb2_spin

; __device__ __forceinline__ int fresh_tid(int wave) { return wave * 64 + fresh_lane(); }
; __device__ __forceinline__ unsigned xb_ld(unsigned* p)              { return __hip_atomic_load(p, __ATOMIC_RELAXED, __HIP_MEMORY_SCOPE_AGENT); }
; __device__ __forceinline__ unsigned xb_xcc_id() { return (unsigned)__builtin_amdgcn_s_getreg((3 << 11) | 20) & 0xFu; }
; __device__ __forceinline__ void xcd_barrier_complete(unsigned* bar, unsigned x, unsigned& nloc, unsigned& nx) {
;     const unsigned G = gridDim.x * gridDim.y * gridDim.z;
;     unsigned sum, cnt, mine, sp = 0u;
;     for (;;) {
;         sum = 0u; cnt = 0u; mine = 0u;
; #pragma unroll
;         for (unsigned j = 0; j < 16; ++j) { const unsigned c = xb_ld(&bar[XB_XCNT(j)]); sum += c; cnt += (c > 0u) ? 1u : 0u; mine = (j == x) ? c : mine; }
;         if (sum == G) break;
;         __builtin_amdgcn_s_sleep(1);
;         if ((++sp & 255u) == 0u) { if (xb_ld(&bar[XB_TMO])) break; if (sp > XB_SPIN_CAP) { atomicAdd(&bar[XB_TMO], 1u); break; } }
;     }
;     nloc = mine > 0u ? mine : 1u; nx = cnt > 0u ? cnt : 1u;
; }
; __device__ __forceinline__ void xcd_barrier(const XcdBarrier& b) {
;     ...
;     if (fresh_tid(b.wave) == 0) {
;         unsigned* bar = b.bar; asm volatile("" : "+s"(bar));
;         __builtin_amdgcn_s_waitcnt(0);
;         const unsigned bx = xb_xcc_id();
;         unsigned nloc = b.st[0], nx = b.st[1];
;         if (nloc == 0u) { xcd_barrier_complete(bar, bx, nloc, nx); b.st[0] = nloc; b.st[1] = nx; }
.Lgb2_orig:
	v_readlane_b32 s36, v253, 53
	v_readlane_b32 s3, v254, 8
	v_readlane_b32 s37, v253, 54
	s_waitcnt vmcnt(0) expcnt(0) lgkmcnt(0)
	v_mov_b32_e32 v0, s3
	s_getreg_b32 s2, hwreg(HW_REG_XCC_ID, 0, 4)
	ds_read_b32 v2, v0
	v_readlane_b32 s3, v254, 9
	s_and_b32 s33, s2, 15
	s_waitcnt lgkmcnt(0)
	v_cmp_ne_u32_e32 vcc, 0, v2
	v_mov_b32_e32 v0, s3
	ds_read_b32 v0, v0
	s_cbranch_vccnz .LBB0_477
	v_readlane_b32 s2, v253, 3
	v_readlane_b32 s3, v253, 4
	s_load_dwordx2 s[6:7], s[2:3], 0x4
	s_add_u32 s2, s36, 0x1000
	s_addc_u32 s3, s37, 0
	s_add_u32 s4, s36, 0x1100
	s_addc_u32 s5, s37, 0
	s_waitcnt lgkmcnt(0)
	s_mul_i32 s28, s6, s78
	s_add_u32 s6, s36, 0x1200
	s_mul_i32 s28, s28, s7
	s_addc_u32 s7, s37, 0
	s_add_u32 s8, s36, 0x1300
	s_addc_u32 s9, s37, 0
	s_mov_b32 s29, 1
	s_mov_b64 s[10:11], 0
	s_branch .LBB0_467

; __device__ __forceinline__ int fresh_tid(int wave) { return wave * 64 + fresh_lane(); }
; __device__ __forceinline__ unsigned xb_ld(unsigned* p)              { return __hip_atomic_load(p, __ATOMIC_RELAXED, __HIP_MEMORY_SCOPE_AGENT); }
; __device__ __forceinline__ unsigned xb_add(unsigned* p, unsigned v) { return __hip_atomic_fetch_add(p, v, __ATOMIC_RELAXED, __HIP_MEMORY_SCOPE_AGENT); }
; __device__ __forceinline__ unsigned xb_xcc_id() { return (unsigned)__builtin_amdgcn_s_getreg((3 << 11) | 20) & 0xFu; }
; #define XB_SPIN(cond, bar) do { unsigned _sp = 0; while (cond) { __builtin_amdgcn_s_sleep(1); \
;     if ((++_sp & 255u) == 0u) { if (xb_ld(&(bar)[XB_TMO])) break; if (_sp > XB_SPIN_CAP) { atomicAdd(&(bar)[XB_TMO], 1u); break; } } } } while (0)
; __device__ __forceinline__ void xcd_barrier(const XcdBarrier& b) {
;     ...
;     if (fresh_tid(b.wave) == 0) {
;         unsigned* bar = b.bar; asm volatile("" : "+s"(bar));
;         __builtin_amdgcn_s_waitcnt(0);
;         const unsigned bx = xb_xcc_id();
;         unsigned nloc = b.st[0], nx = b.st[1];
;         if (nloc == 0u) { xcd_barrier_complete(bar, bx, nloc, nx); b.st[0] = nloc; b.st[1] = nx; }
;         const unsigned old = xb_add(&bar[XB_XSUB(bx)], 1u);
;         const unsigned gen = old / nloc;
;         if (old + 1u == (gen + 1u) * nloc) {
;             __builtin_amdgcn_fence(__ATOMIC_RELEASE, "agent");
;             asm volatile("s_waitcnt vmcnt(0)" ::: "memory");
;             const unsigned og = xb_add(&bar[XB_TOP], 1u);
;             const unsigned tg = og / nx;
;             if (og + 1u == (tg + 1u) * nx) xb_add(&bar[XB_TOPGEN], 1u);
;             else XB_SPIN(xb_ld(&bar[XB_TOPGEN]) == tg, bar);
;             __builtin_amdgcn_fence(__ATOMIC_ACQUIRE, "agent");
;             xb_add(&bar[XB_XGEN(bx)], 1u);
;             asm volatile("s_waitcnt vmcnt(0)" ::: "memory");
;         } else {
;             XB_SPIN(xb_ld(&bar[XB_XGEN(bx)]) == gen, bar);
;             __builtin_amdgcn_fence(__ATOMIC_ACQUIRE, "agent");
;             asm volatile("s_waitcnt vmcnt(0)" ::: "memory");
;         }
.LBB0_903:
	s_mov_b32 s0, s93
	s_waitcnt vmcnt(0) lgkmcnt(0)
	s_barrier
	s_waitcnt vmcnt(0)
	s_barrier
	s_nop 0
	v_mbcnt_lo_u32_b32 v0, -1, s0
	v_mbcnt_hi_u32_b32 v0, -1, v0
	v_readlane_b32 s0, v254, 17
	s_nop 1
	v_cmp_eq_u32_e32 vcc, s0, v0
	s_and_saveexec_b64 s[0:1], vcc
	s_cbranch_execz .LBB0_947
	s_bitcmp1_b32 s100, 0
	s_cbranch_scc0 .Lgb3_orig
	v_readlane_b32 s2, v253, 53
	v_readlane_b32 s3, v253, 54
	s_getreg_b32 s4, hwreg(HW_REG_XCC_ID, 0, 4)
	v_mov_b32_e32 v1, 1
	s_and_b32 s4, s4, 15
	s_lshl_b32 s4, s4, 8
	s_addk_i32 s4, 0x1400
	v_mov_b32_e32 v0, s4
	s_waitcnt vmcnt(0) lgkmcnt(0)
	global_atomic_add v2, v0, v1, s[2:3] sc0
	s_waitcnt vmcnt(0)
	v_readfirstlane_b32 s4, v2
	s_lshr_b32 s5, s4, 5
	s_and_b32 s4, s4, 31
	s_add_i32 s5, s5, 1
	s_lshl_b32 s5, s5, 3
	s_cmp_lg_u32 s4, 31
	s_cbranch_scc1 .Lgb3_poll
	buffer_wbl2 sc1
	s_waitcnt vmcnt(0)
	v_add_u32_e32 v0, 0x1000, v0
	global_atomic_add v0, v1, s[2:3]
	v_mov_b32_e32 v0, 0x3400
	global_atomic_add v2, v0, v1, s[2:3] sc0
	s_waitcnt vmcnt(0)
	v_readfirstlane_b32 s4, v2
	s_add_i32 s4, s4, 1
	s_cmp_lg_u32 s4, s5
	s_cbranch_scc1 .Lgb3_poll
	v_mov_b32_e32 v0, 0x3500
	global_atomic_add v0, v1, s[2:3]
	s_branch .Lgb3_done
.Lgb3_poll:
	v_mov_b32_e32 v0, 0x3400
	s_mov_b32 s4, 0
.Lgb3_spin:
	global_load_dword v3, v0, s[2:3] sc1
	s_waitcnt vmcnt(0)
	v_subrev_u32_e32 v3, s5, v3
	v_cmp_gt_i32_e32 vcc, 0, v3
	s_cbranch_vccz .Lgb3_done
	s_sleep 1
	s_add_i32 s4, s4, 1
	s_cmp_lt_u32 s4, 0x100000
	s_cbranch_scc1 .Lgb3_spin

; __device__ __forceinline__ int fresh_tid(int wave) { return wave * 64 + fresh_lane(); }
; __device__ __forceinline__ unsigned xb_ld(unsigned* p)              { return __hip_atomic_load(p, __ATOMIC_RELAXED, __HIP_MEMORY_SCOPE_AGENT); }
; __device__ __forceinline__ unsigned xb_add(unsigned* p, unsigned v) { return __hip_atomic_fetch_add(p, v, __ATOMIC_RELAXED, __HIP_MEMORY_SCOPE_AGENT); }
; __device__ __forceinline__ unsigned xb_xcc_id() { return (unsigned)__builtin_amdgcn_s_getreg((3 << 11) | 20) & 0xFu; }
; #define XB_SPIN(cond, bar) do { unsigned _sp = 0; while (cond) { __builtin_amdgcn_s_sleep(1); \
;     if ((++_sp & 255u) == 0u) { if (xb_ld(&(bar)[XB_TMO])) break; if (_sp > XB_SPIN_CAP) { atomicAdd(&(bar)[XB_TMO], 1u); break; } } } } while (0)
; __device__ __forceinline__ void xcd_barrier(const XcdBarrier& b) {
;     ...
;     if (fresh_tid(b.wave) == 0) {
;         unsigned* bar = b.bar; asm volatile("" : "+s"(bar));
;         __builtin_amdgcn_s_waitcnt(0);
;         const unsigned bx = xb_xcc_id();
;         unsigned nloc = b.st[0], nx = b.st[1];
;         if (nloc == 0u) { xcd_barrier_complete(bar, bx, nloc, nx); b.st[0] = nloc; b.st[1] = nx; }
;         const unsigned old = xb_add(&bar[XB_XSUB(bx)], 1u);
;         const unsigned gen = old / nloc;
;         if (old + 1u == (gen + 1u) * nloc) {
;             __builtin_amdgcn_fence(__ATOMIC_RELEASE, "agent");
;             asm volatile("s_waitcnt vmcnt(0)" ::: "memory");
;             const unsigned og = xb_add(&bar[XB_TOP], 1u);
;             const unsigned tg = og / nx;
;             if (og + 1u == (tg + 1u) * nx) xb_add(&bar[XB_TOPGEN], 1u);
;             else XB_SPIN(xb_ld(&bar[XB_TOPGEN]) == tg, bar);
;             __builtin_amdgcn_fence(__ATOMIC_ACQUIRE, "agent");
;             xb_add(&bar[XB_XGEN(bx)], 1u);
;             asm volatile("s_waitcnt vmcnt(0)" ::: "memory");
;         } else {
;             XB_SPIN(xb_ld(&bar[XB_XGEN(bx)]) == gen, bar);
;             __builtin_amdgcn_fence(__ATOMIC_ACQUIRE, "agent");
;             asm volatile("s_waitcnt vmcnt(0)" ::: "memory");
;         }
.LBB0_1323:
	s_mov_b32 s0, s93
	s_waitcnt vmcnt(0)
	s_waitcnt lgkmcnt(0)
	s_barrier
	s_nop 0
	v_mbcnt_lo_u32_b32 v0, -1, s0
	v_mbcnt_hi_u32_b32 v0, -1, v0
	v_readlane_b32 s0, v254, 17
	s_nop 1
	v_cmp_eq_u32_e32 vcc, s0, v0
	s_and_saveexec_b64 s[0:1], vcc
	s_cbranch_execz .LBB0_1367
	s_bitcmp1_b32 s100, 0
	s_cbranch_scc0 .Lgb4_orig
	v_readlane_b32 s2, v253, 53
	v_readlane_b32 s3, v253, 54
	s_getreg_b32 s4, hwreg(HW_REG_XCC_ID, 0, 4)
	v_mov_b32_e32 v1, 1
	s_and_b32 s4, s4, 15
	s_lshl_b32 s4, s4, 8
	s_addk_i32 s4, 0x1400
	v_mov_b32_e32 v0, s4
	s_waitcnt vmcnt(0) lgkmcnt(0)
	global_atomic_add v2, v0, v1, s[2:3] sc0
	s_waitcnt vmcnt(0)
	v_readfirstlane_b32 s4, v2
	s_lshr_b32 s5, s4, 5
	s_and_b32 s4, s4, 31
	s_add_i32 s5, s5, 1
	s_lshl_b32 s5, s5, 3
	s_cmp_lg_u32 s4, 31
	s_cbranch_scc1 .Lgb4_poll
	buffer_wbl2 sc1
	s_waitcnt vmcnt(0)
	v_add_u32_e32 v0, 0x1000, v0
	global_atomic_add v0, v1, s[2:3]
	v_mov_b32_e32 v0, 0x3400
	global_atomic_add v2, v0, v1, s[2:3] sc0
	s_waitcnt vmcnt(0)
	v_readfirstlane_b32 s4, v2
	s_add_i32 s4, s4, 1
	s_cmp_lg_u32 s4, s5
	s_cbranch_scc1 .Lgb4_poll
	v_mov_b32_e32 v0, 0x3500
	global_atomic_add v0, v1, s[2:3]
	s_branch .Lgb4_done

; __device__ __forceinline__ int fresh_tid(int wave) { return wave * 64 + fresh_lane(); }
; __device__ __forceinline__ unsigned xb_ld(unsigned* p)              { return __hip_atomic_load(p, __ATOMIC_RELAXED, __HIP_MEMORY_SCOPE_AGENT); }
; __device__ __forceinline__ unsigned xb_add(unsigned* p, unsigned v) { return __hip_atomic_fetch_add(p, v, __ATOMIC_RELAXED, __HIP_MEMORY_SCOPE_AGENT); }
; __device__ __forceinline__ unsigned xb_xcc_id() { return (unsigned)__builtin_amdgcn_s_getreg((3 << 11) | 20) & 0xFu; }
; #define XB_SPIN(cond, bar) do { unsigned _sp = 0; while (cond) { __builtin_amdgcn_s_sleep(1); \
;     if ((++_sp & 255u) == 0u) { if (xb_ld(&(bar)[XB_TMO])) break; if (_sp > XB_SPIN_CAP) { atomicAdd(&(bar)[XB_TMO], 1u); break; } } } } while (0)
; __device__ __forceinline__ void xcd_barrier(const XcdBarrier& b) {
;     ...
;     if (fresh_tid(b.wave) == 0) {
;         unsigned* bar = b.bar; asm volatile("" : "+s"(bar));
;         __builtin_amdgcn_s_waitcnt(0);
;         const unsigned bx = xb_xcc_id();
;         unsigned nloc = b.st[0], nx = b.st[1];
;         if (nloc == 0u) { xcd_barrier_complete(bar, bx, nloc, nx); b.st[0] = nloc; b.st[1] = nx; }
;         const unsigned old = xb_add(&bar[XB_XSUB(bx)], 1u);
;         const unsigned gen = old / nloc;
;         if (old + 1u == (gen + 1u) * nloc) {
;             __builtin_amdgcn_fence(__ATOMIC_RELEASE, "agent");
;             asm volatile("s_waitcnt vmcnt(0)" ::: "memory");
;             const unsigned og = xb_add(&bar[XB_TOP], 1u);
;             const unsigned tg = og / nx;
;             if (og + 1u == (tg + 1u) * nx) xb_add(&bar[XB_TOPGEN], 1u);
;             else XB_SPIN(xb_ld(&bar[XB_TOPGEN]) == tg, bar);
;             __builtin_amdgcn_fence(__ATOMIC_ACQUIRE, "agent");
;             xb_add(&bar[XB_XGEN(bx)], 1u);
;             asm volatile("s_waitcnt vmcnt(0)" ::: "memory");
;         } else {
;             XB_SPIN(xb_ld(&bar[XB_XGEN(bx)]) == gen, bar);
;             __builtin_amdgcn_fence(__ATOMIC_ACQUIRE, "agent");
;             asm volatile("s_waitcnt vmcnt(0)" ::: "memory");
;         }
.LBB0_1402:
	s_mov_b32 s1, s93
	s_waitcnt vmcnt(0)
	s_waitcnt lgkmcnt(0)
	s_barrier
	s_nop 0
	v_mbcnt_lo_u32_b32 v0, -1, s1
	v_mbcnt_hi_u32_b32 v0, -1, v0
	v_readlane_b32 s1, v254, 17
	s_nop 1
	v_cmp_eq_u32_e32 vcc, s1, v0
	s_and_saveexec_b64 s[42:43], vcc
	s_mov_b32 s33, 0x42fe0000
	s_movk_i32 s60, 0x3800
	s_mov_b32 s61, 0xc0c0500
	s_mov_b32 s62, 0x43800000
	s_cbranch_execz .LBB0_1446
	s_bitcmp1_b32 s100, 0
	s_cbranch_scc0 .Lgb5_orig
	v_readlane_b32 s44, v253, 53
	v_readlane_b32 s45, v253, 54
	s_getreg_b32 s1, hwreg(HW_REG_XCC_ID, 0, 4)
	v_mov_b32_e32 v1, 1
	s_and_b32 s1, s1, 15
	s_lshl_b32 s1, s1, 8
	s_addk_i32 s1, 0x1400
	v_mov_b32_e32 v0, s1
	s_waitcnt vmcnt(0) lgkmcnt(0)
	global_atomic_add v2, v0, v1, s[44:45] sc0
	s_waitcnt vmcnt(0)
	v_readfirstlane_b32 s1, v2
	s_lshr_b32 s4, s1, 5
	s_and_b32 s1, s1, 31
	s_add_i32 s4, s4, 1
	s_lshl_b32 s4, s4, 3
	s_cmp_lg_u32 s1, 31
	s_cbranch_scc1 .Lgb5_poll
	buffer_wbl2 sc1
	s_waitcnt vmcnt(0)
	v_add_u32_e32 v0, 0x1000, v0
	global_atomic_add v0, v1, s[44:45]
	v_mov_b32_e32 v0, 0x3400
	global_atomic_add v2, v0, v1, s[44:45] sc0
	s_waitcnt vmcnt(0)
	v_readfirstlane_b32 s1, v2
	s_add_i32 s1, s1, 1
	s_cmp_lg_u32 s1, s4
	s_cbranch_scc1 .Lgb5_poll
	v_mov_b32_e32 v0, 0x3500
	global_atomic_add v0, v1, s[44:45]
	s_branch .Lgb5_done
.Lgb5_poll:
	v_mov_b32_e32 v0, 0x3400
	s_mov_b32 s1, 0
.Lgb5_spin:
	global_load_dword v3, v0, s[44:45] sc1
	s_waitcnt vmcnt(0)
	v_subrev_u32_e32 v3, s4, v3
	v_cmp_gt_i32_e32 vcc, 0, v3
	s_cbranch_vccz .Lgb5_done
	s_sleep 1
	s_add_i32 s1, s1, 1
	s_cmp_lt_u32 s1, 0x100000
	s_cbranch_scc1 .Lgb5_spin

; __device__ __forceinline__ int fresh_tid(int wave) { return wave * 64 + fresh_lane(); }
; __device__ __forceinline__ unsigned xb_ld(unsigned* p)              { return __hip_atomic_load(p, __ATOMIC_RELAXED, __HIP_MEMORY_SCOPE_AGENT); }
; __device__ __forceinline__ unsigned xb_xcc_id() { return (unsigned)__builtin_amdgcn_s_getreg((3 << 11) | 20) & 0xFu; }
; __device__ __forceinline__ void xcd_barrier_complete(unsigned* bar, unsigned x, unsigned& nloc, unsigned& nx) {
;     const unsigned G = gridDim.x * gridDim.y * gridDim.z;
;     unsigned sum, cnt, mine, sp = 0u;
;     for (;;) {
;         sum = 0u; cnt = 0u; mine = 0u;
; #pragma unroll
;         for (unsigned j = 0; j < 16; ++j) { const unsigned c = xb_ld(&bar[XB_XCNT(j)]); sum += c; cnt += (c > 0u) ? 1u : 0u; mine = (j == x) ? c : mine; }
;         if (sum == G) break;
;         __builtin_amdgcn_s_sleep(1);
;         if ((++sp & 255u) == 0u) { if (xb_ld(&bar[XB_TMO])) break; if (sp > XB_SPIN_CAP) { atomicAdd(&bar[XB_TMO], 1u); break; } }
;     }
;     nloc = mine > 0u ? mine : 1u; nx = cnt > 0u ? cnt : 1u;
; }
; __device__ __forceinline__ void xcd_barrier(const XcdBarrier& b) {
;     ...
;     if (fresh_tid(b.wave) == 0) {
;         unsigned* bar = b.bar; asm volatile("" : "+s"(bar));
;         __builtin_amdgcn_s_waitcnt(0);
;         const unsigned bx = xb_xcc_id();
;         unsigned nloc = b.st[0], nx = b.st[1];
;         if (nloc == 0u) { xcd_barrier_complete(bar, bx, nloc, nx); b.st[0] = nloc; b.st[1] = nx; }
.Lgb5_orig:
	v_readlane_b32 s44, v253, 53
	v_readlane_b32 s4, v254, 8
	v_readlane_b32 s45, v253, 54
	s_waitcnt vmcnt(0) expcnt(0) lgkmcnt(0)
	v_mov_b32_e32 v0, s4
	s_getreg_b32 s1, hwreg(HW_REG_XCC_ID, 0, 4)
	ds_read_b32 v2, v0
	v_readlane_b32 s4, v254, 9
	s_and_b32 s1, s1, 15
	s_waitcnt lgkmcnt(0)
	v_cmp_ne_u32_e32 vcc, 0, v2
	v_mov_b32_e32 v0, s4
	ds_read_b32 v0, v0
	s_cbranch_vccnz .LBB0_1417
	v_readlane_b32 s4, v253, 3
	v_readlane_b32 s5, v253, 4
	s_load_dwordx2 s[8:9], s[4:5], 0x4
	s_add_u32 s4, s44, 0x1000
	s_addc_u32 s5, s45, 0
	s_add_u32 s6, s44, 0x1100
	s_addc_u32 s7, s45, 0
	s_waitcnt lgkmcnt(0)
	s_mul_i32 s30, s8, s78
	s_add_u32 s8, s44, 0x1200
	s_mul_i32 s30, s30, s9
	s_addc_u32 s9, s45, 0
	s_add_u32 s10, s44, 0x1300
	s_addc_u32 s11, s45, 0
	s_mov_b32 s31, 1
	s_mov_b64 s[12:13], 0
	s_branch .LBB0_1407

; __device__ __forceinline__ int fresh_tid(int wave) { return wave * 64 + fresh_lane(); }
; __device__ __forceinline__ unsigned xb_ld(unsigned* p)              { return __hip_atomic_load(p, __ATOMIC_RELAXED, __HIP_MEMORY_SCOPE_AGENT); }
; __device__ __forceinline__ unsigned xb_add(unsigned* p, unsigned v) { return __hip_atomic_fetch_add(p, v, __ATOMIC_RELAXED, __HIP_MEMORY_SCOPE_AGENT); }
; __device__ __forceinline__ unsigned xb_xcc_id() { return (unsigned)__builtin_amdgcn_s_getreg((3 << 11) | 20) & 0xFu; }
; #define XB_SPIN(cond, bar) do { unsigned _sp = 0; while (cond) { __builtin_amdgcn_s_sleep(1); \
;     if ((++_sp & 255u) == 0u) { if (xb_ld(&(bar)[XB_TMO])) break; if (_sp > XB_SPIN_CAP) { atomicAdd(&(bar)[XB_TMO], 1u); break; } } } } while (0)
; __device__ __forceinline__ void xcd_barrier(const XcdBarrier& b) {
;     ...
;     if (fresh_tid(b.wave) == 0) {
;         unsigned* bar = b.bar; asm volatile("" : "+s"(bar));
;         __builtin_amdgcn_s_waitcnt(0);
;         const unsigned bx = xb_xcc_id();
;         unsigned nloc = b.st[0], nx = b.st[1];
;         if (nloc == 0u) { xcd_barrier_complete(bar, bx, nloc, nx); b.st[0] = nloc; b.st[1] = nx; }
;         const unsigned old = xb_add(&bar[XB_XSUB(bx)], 1u);
;         const unsigned gen = old / nloc;
;         if (old + 1u == (gen + 1u) * nloc) {
;             __builtin_amdgcn_fence(__ATOMIC_RELEASE, "agent");
;             asm volatile("s_waitcnt vmcnt(0)" ::: "memory");
;             const unsigned og = xb_add(&bar[XB_TOP], 1u);
;             const unsigned tg = og / nx;
;             if (og + 1u == (tg + 1u) * nx) xb_add(&bar[XB_TOPGEN], 1u);
;             else XB_SPIN(xb_ld(&bar[XB_TOPGEN]) == tg, bar);
;             __builtin_amdgcn_fence(__ATOMIC_ACQUIRE, "agent");
;             xb_add(&bar[XB_XGEN(bx)], 1u);
;             asm volatile("s_waitcnt vmcnt(0)" ::: "memory");
;         } else {
;             XB_SPIN(xb_ld(&bar[XB_XGEN(bx)]) == gen, bar);
;             __builtin_amdgcn_fence(__ATOMIC_ACQUIRE, "agent");
;             asm volatile("s_waitcnt vmcnt(0)" ::: "memory");
;         }
.LBB0_1472:
	s_mov_b32 s0, s93
	s_waitcnt vmcnt(0)
	s_waitcnt lgkmcnt(0)
	s_barrier
	s_nop 0
	v_mbcnt_lo_u32_b32 v0, -1, s0
	v_mbcnt_hi_u32_b32 v0, -1, v0
	v_readlane_b32 s0, v254, 17
	s_nop 1
	v_cmp_eq_u32_e32 vcc, s0, v0
	s_and_saveexec_b64 s[0:1], vcc
	s_cbranch_execz .LBB0_1516
	s_bitcmp1_b32 s100, 0
	s_cbranch_scc0 .Lgb6_orig
	v_readlane_b32 s34, v253, 53
	v_readlane_b32 s35, v253, 54
	s_getreg_b32 s2, hwreg(HW_REG_XCC_ID, 0, 4)
	v_mov_b32_e32 v1, 1
	s_and_b32 s2, s2, 15
	s_lshl_b32 s2, s2, 8
	s_addk_i32 s2, 0x1400
	v_mov_b32_e32 v0, s2
	s_waitcnt vmcnt(0) lgkmcnt(0)
	global_atomic_add v2, v0, v1, s[34:35] sc0
	s_waitcnt vmcnt(0)
	v_readfirstlane_b32 s2, v2
	s_lshr_b32 s3, s2, 5
	s_and_b32 s2, s2, 31
	s_add_i32 s3, s3, 1
	s_lshl_b32 s3, s3, 3
	s_cmp_lg_u32 s2, 31
	s_cbranch_scc1 .Lgb6_poll
	buffer_wbl2 sc1
	s_waitcnt vmcnt(0)
	v_add_u32_e32 v0, 0x1000, v0
	global_atomic_add v0, v1, s[34:35]
	v_mov_b32_e32 v0, 0x3400
	global_atomic_add v2, v0, v1, s[34:35] sc0
	s_waitcnt vmcnt(0)
	v_readfirstlane_b32 s2, v2
	s_add_i32 s2, s2, 1
	s_cmp_lg_u32 s2, s3
	s_cbranch_scc1 .Lgb6_poll
	v_mov_b32_e32 v0, 0x3500
	global_atomic_add v0, v1, s[34:35]
	s_branch .Lgb6_done

; __device__ __forceinline__ unsigned xb_ld(unsigned* p)              { return __hip_atomic_load(p, __ATOMIC_RELAXED, __HIP_MEMORY_SCOPE_AGENT); }
; __device__ __forceinline__ unsigned xb_add(unsigned* p, unsigned v) { return __hip_atomic_fetch_add(p, v, __ATOMIC_RELAXED, __HIP_MEMORY_SCOPE_AGENT); }
; #define XB_SPIN(cond, bar) do { unsigned _sp = 0; while (cond) { __builtin_amdgcn_s_sleep(1); \
;     if ((++_sp & 255u) == 0u) { if (xb_ld(&(bar)[XB_TMO])) break; if (_sp > XB_SPIN_CAP) { atomicAdd(&(bar)[XB_TMO], 1u); break; } } } } while (0)
; __device__ __forceinline__ void xcd_barrier(const XcdBarrier& b) {
;     ...
;             else XB_SPIN(xb_ld(&bar[XB_TOPGEN]) == tg, bar);
;             __builtin_amdgcn_fence(__ATOMIC_ACQUIRE, "agent");
;             xb_add(&bar[XB_XGEN(bx)], 1u);
;             asm volatile("s_waitcnt vmcnt(0)" ::: "memory");
;         } else {
;             XB_SPIN(xb_ld(&bar[XB_XGEN(bx)]) == gen, bar);
.Lgb6_spin:
	global_load_dword v3, v0, s[34:35] sc1
	s_waitcnt vmcnt(0)
	v_subrev_u32_e32 v3, s3, v3
	v_cmp_gt_i32_e32 vcc, 0, v3
	s_cbranch_vccz .Lgb6_done
	s_sleep 1
	s_add_i32 s2, s2, 1
	s_cmp_lt_u32 s2, 0x100000
	s_cbranch_scc1 .Lgb6_spin

; __device__ __forceinline__ int fresh_tid(int wave) { return wave * 64 + fresh_lane(); }
; __device__ __forceinline__ unsigned xb_ld(unsigned* p)              { return __hip_atomic_load(p, __ATOMIC_RELAXED, __HIP_MEMORY_SCOPE_AGENT); }
; __device__ __forceinline__ unsigned xb_xcc_id() { return (unsigned)__builtin_amdgcn_s_getreg((3 << 11) | 20) & 0xFu; }
; __device__ __forceinline__ void xcd_barrier_complete(unsigned* bar, unsigned x, unsigned& nloc, unsigned& nx) {
;     const unsigned G = gridDim.x * gridDim.y * gridDim.z;
;     unsigned sum, cnt, mine, sp = 0u;
;     for (;;) {
;         sum = 0u; cnt = 0u; mine = 0u;
; #pragma unroll
;         for (unsigned j = 0; j < 16; ++j) { const unsigned c = xb_ld(&bar[XB_XCNT(j)]); sum += c; cnt += (c > 0u) ? 1u : 0u; mine = (j == x) ? c : mine; }
;         if (sum == G) break;
;         __builtin_amdgcn_s_sleep(1);
;         if ((++sp & 255u) == 0u) { if (xb_ld(&bar[XB_TMO])) break; if (sp > XB_SPIN_CAP) { atomicAdd(&bar[XB_TMO], 1u); break; } }
;     }
;     nloc = mine > 0u ? mine : 1u; nx = cnt > 0u ? cnt : 1u;
; }
; __device__ __forceinline__ void xcd_barrier(const XcdBarrier& b) {
;     ...
;     if (fresh_tid(b.wave) == 0) {
;         unsigned* bar = b.bar; asm volatile("" : "+s"(bar));
;         __builtin_amdgcn_s_waitcnt(0);
;         const unsigned bx = xb_xcc_id();
;         unsigned nloc = b.st[0], nx = b.st[1];
;         if (nloc == 0u) { xcd_barrier_complete(bar, bx, nloc, nx); b.st[0] = nloc; b.st[1] = nx; }
.Lgb6_orig:
	v_readlane_b32 s34, v253, 53
	v_readlane_b32 s3, v254, 8
	v_readlane_b32 s35, v253, 54
	s_waitcnt vmcnt(0) expcnt(0) lgkmcnt(0)
	v_mov_b32_e32 v0, s3
	s_getreg_b32 s2, hwreg(HW_REG_XCC_ID, 0, 4)
	ds_read_b32 v2, v0
	v_readlane_b32 s3, v254, 9
	s_and_b32 s33, s2, 15
	s_waitcnt lgkmcnt(0)
	v_cmp_ne_u32_e32 vcc, 0, v2
	v_mov_b32_e32 v0, s3
	ds_read_b32 v0, v0
	s_cbranch_vccnz .LBB0_1487
	v_readlane_b32 s2, v253, 3
	v_readlane_b32 s3, v253, 4
	s_load_dwordx2 s[6:7], s[2:3], 0x4
	s_add_u32 s2, s34, 0x1000
	s_addc_u32 s3, s35, 0
	s_add_u32 s4, s34, 0x1100
	s_addc_u32 s5, s35, 0
	s_waitcnt lgkmcnt(0)
	s_mul_i32 s28, s6, s78
	s_add_u32 s6, s34, 0x1200
	s_mul_i32 s28, s28, s7
	s_addc_u32 s7, s35, 0
	s_add_u32 s8, s34, 0x1300
	s_addc_u32 s9, s35, 0
	s_mov_b32 s29, 1
	s_mov_b64 s[10:11], 0
	s_branch .LBB0_1477

; __device__ __forceinline__ int fresh_tid(int wave) { return wave * 64 + fresh_lane(); }
; __device__ __forceinline__ unsigned xb_ld(unsigned* p)              { return __hip_atomic_load(p, __ATOMIC_RELAXED, __HIP_MEMORY_SCOPE_AGENT); }
; __device__ __forceinline__ unsigned xb_add(unsigned* p, unsigned v) { return __hip_atomic_fetch_add(p, v, __ATOMIC_RELAXED, __HIP_MEMORY_SCOPE_AGENT); }
; __device__ __forceinline__ unsigned xb_xcc_id() { return (unsigned)__builtin_amdgcn_s_getreg((3 << 11) | 20) & 0xFu; }
; #define XB_SPIN(cond, bar) do { unsigned _sp = 0; while (cond) { __builtin_amdgcn_s_sleep(1); \
;     if ((++_sp & 255u) == 0u) { if (xb_ld(&(bar)[XB_TMO])) break; if (_sp > XB_SPIN_CAP) { atomicAdd(&(bar)[XB_TMO], 1u); break; } } } } while (0)
; __device__ __forceinline__ void xcd_barrier(const XcdBarrier& b) {
;     ...
;     if (fresh_tid(b.wave) == 0) {
;         unsigned* bar = b.bar; asm volatile("" : "+s"(bar));
;         __builtin_amdgcn_s_waitcnt(0);
;         const unsigned bx = xb_xcc_id();
;         unsigned nloc = b.st[0], nx = b.st[1];
;         if (nloc == 0u) { xcd_barrier_complete(bar, bx, nloc, nx); b.st[0] = nloc; b.st[1] = nx; }
;         const unsigned old = xb_add(&bar[XB_XSUB(bx)], 1u);
;         const unsigned gen = old / nloc;
;         if (old + 1u == (gen + 1u) * nloc) {
;             __builtin_amdgcn_fence(__ATOMIC_RELEASE, "agent");
;             asm volatile("s_waitcnt vmcnt(0)" ::: "memory");
;             const unsigned og = xb_add(&bar[XB_TOP], 1u);
;             const unsigned tg = og / nx;
;             if (og + 1u == (tg + 1u) * nx) xb_add(&bar[XB_TOPGEN], 1u);
;             else XB_SPIN(xb_ld(&bar[XB_TOPGEN]) == tg, bar);
;             __builtin_amdgcn_fence(__ATOMIC_ACQUIRE, "agent");
;             xb_add(&bar[XB_XGEN(bx)], 1u);
;             asm volatile("s_waitcnt vmcnt(0)" ::: "memory");
;         } else {
;             XB_SPIN(xb_ld(&bar[XB_XGEN(bx)]) == gen, bar);
;             __builtin_amdgcn_fence(__ATOMIC_ACQUIRE, "agent");
;             asm volatile("s_waitcnt vmcnt(0)" ::: "memory");
;         }
.LBB0_1569:
	s_mov_b32 s0, s93
	s_waitcnt vmcnt(0)
	s_waitcnt lgkmcnt(0)
	s_barrier
	s_nop 0
	v_mbcnt_lo_u32_b32 v0, -1, s0
	v_mbcnt_hi_u32_b32 v0, -1, v0
	v_readlane_b32 s0, v254, 17
	s_nop 1
	v_cmp_eq_u32_e32 vcc, s0, v0
	s_and_saveexec_b64 s[0:1], vcc
	s_cbranch_execz .LBB0_1613
	s_bitcmp1_b32 s100, 0
	s_cbranch_scc0 .Lgb7_orig
	v_readlane_b32 s64, v253, 53
	v_readlane_b32 s65, v253, 54
	s_getreg_b32 s2, hwreg(HW_REG_XCC_ID, 0, 4)
	v_mov_b32_e32 v1, 1
	s_and_b32 s2, s2, 15
	s_lshl_b32 s2, s2, 8
	s_addk_i32 s2, 0x1400
	v_mov_b32_e32 v0, s2
	s_waitcnt vmcnt(0) lgkmcnt(0)
	global_atomic_add v2, v0, v1, s[64:65] sc0
	s_waitcnt vmcnt(0)
	v_readfirstlane_b32 s2, v2
	s_lshr_b32 s3, s2, 5
	s_and_b32 s2, s2, 31
	s_add_i32 s3, s3, 1
	s_lshl_b32 s3, s3, 3
	s_cmp_lg_u32 s2, 31
	s_cbranch_scc1 .Lgb7_poll
	buffer_wbl2 sc1
	s_waitcnt vmcnt(0)
	v_add_u32_e32 v0, 0x1000, v0
	global_atomic_add v0, v1, s[64:65]
	v_mov_b32_e32 v0, 0x3400
	global_atomic_add v2, v0, v1, s[64:65] sc0
	s_waitcnt vmcnt(0)
	v_readfirstlane_b32 s2, v2
	s_add_i32 s2, s2, 1
	s_cmp_lg_u32 s2, s3
	s_cbranch_scc1 .Lgb7_poll
	v_mov_b32_e32 v0, 0x3500
	global_atomic_add v0, v1, s[64:65]
	s_branch .Lgb7_done

; __device__ __forceinline__ unsigned xb_ld(unsigned* p)              { return __hip_atomic_load(p, __ATOMIC_RELAXED, __HIP_MEMORY_SCOPE_AGENT); }
; __device__ __forceinline__ unsigned xb_add(unsigned* p, unsigned v) { return __hip_atomic_fetch_add(p, v, __ATOMIC_RELAXED, __HIP_MEMORY_SCOPE_AGENT); }
; #define XB_SPIN(cond, bar) do { unsigned _sp = 0; while (cond) { __builtin_amdgcn_s_sleep(1); \
;     if ((++_sp & 255u) == 0u) { if (xb_ld(&(bar)[XB_TMO])) break; if (_sp > XB_SPIN_CAP) { atomicAdd(&(bar)[XB_TMO], 1u); break; } } } } while (0)
; __device__ __forceinline__ void xcd_barrier(const XcdBarrier& b) {
;     ...
;             else XB_SPIN(xb_ld(&bar[XB_TOPGEN]) == tg, bar);
;             __builtin_amdgcn_fence(__ATOMIC_ACQUIRE, "agent");
;             xb_add(&bar[XB_XGEN(bx)], 1u);
;             asm volatile("s_waitcnt vmcnt(0)" ::: "memory");
;         } else {
;             XB_SPIN(xb_ld(&bar[XB_XGEN(bx)]) == gen, bar);
.Lgb7_spin:
	global_load_dword v3, v0, s[64:65] sc1
	s_waitcnt vmcnt(0)
	v_subrev_u32_e32 v3, s3, v3
	v_cmp_gt_i32_e32 vcc, 0, v3
	s_cbranch_vccz .Lgb7_done
	s_sleep 1
	s_add_i32 s2, s2, 1
	s_cmp_lt_u32 s2, 0x100000
	s_cbranch_scc1 .Lgb7_spin

; __device__ __forceinline__ int fresh_tid(int wave) { return wave * 64 + fresh_lane(); }
; __device__ __forceinline__ unsigned xb_ld(unsigned* p)              { return __hip_atomic_load(p, __ATOMIC_RELAXED, __HIP_MEMORY_SCOPE_AGENT); }
; __device__ __forceinline__ unsigned xb_xcc_id() { return (unsigned)__builtin_amdgcn_s_getreg((3 << 11) | 20) & 0xFu; }
; __device__ __forceinline__ void xcd_barrier_complete(unsigned* bar, unsigned x, unsigned& nloc, unsigned& nx) {
;     const unsigned G = gridDim.x * gridDim.y * gridDim.z;
;     unsigned sum, cnt, mine, sp = 0u;
;     for (;;) {
;         sum = 0u; cnt = 0u; mine = 0u;
; #pragma unroll
;         for (unsigned j = 0; j < 16; ++j) { const unsigned c = xb_ld(&bar[XB_XCNT(j)]); sum += c; cnt += (c > 0u) ? 1u : 0u; mine = (j == x) ? c : mine; }
;         if (sum == G) break;
;         __builtin_amdgcn_s_sleep(1);
;         if ((++sp & 255u) == 0u) { if (xb_ld(&bar[XB_TMO])) break; if (sp > XB_SPIN_CAP) { atomicAdd(&bar[XB_TMO], 1u); break; } }
;     }
;     nloc = mine > 0u ? mine : 1u; nx = cnt > 0u ? cnt : 1u;
; }
; __device__ __forceinline__ void xcd_barrier(const XcdBarrier& b) {
;     ...
;     if (fresh_tid(b.wave) == 0) {
;         unsigned* bar = b.bar; asm volatile("" : "+s"(bar));
;         __builtin_amdgcn_s_waitcnt(0);
;         const unsigned bx = xb_xcc_id();
;         unsigned nloc = b.st[0], nx = b.st[1];
;         if (nloc == 0u) { xcd_barrier_complete(bar, bx, nloc, nx); b.st[0] = nloc; b.st[1] = nx; }
.Lgb7_orig:
	v_readlane_b32 s64, v253, 53
	v_readlane_b32 s3, v254, 8
	v_readlane_b32 s65, v253, 54
	s_waitcnt vmcnt(0) expcnt(0) lgkmcnt(0)
	v_mov_b32_e32 v0, s3
	s_getreg_b32 s2, hwreg(HW_REG_XCC_ID, 0, 4)
	ds_read_b32 v2, v0
	v_readlane_b32 s3, v254, 9
	s_and_b32 s33, s2, 15
	s_waitcnt lgkmcnt(0)
	v_cmp_ne_u32_e32 vcc, 0, v2
	v_mov_b32_e32 v0, s3
	ds_read_b32 v0, v0
	s_cbranch_vccnz .LBB0_1584
	v_readlane_b32 s2, v253, 3
	v_readlane_b32 s3, v253, 4
	s_load_dwordx2 s[6:7], s[2:3], 0x4
	s_add_u32 s2, s64, 0x1000
	s_addc_u32 s3, s65, 0
	s_add_u32 s4, s64, 0x1100
	s_addc_u32 s5, s65, 0
	s_waitcnt lgkmcnt(0)
	s_mul_i32 s28, s6, s78
	s_add_u32 s6, s64, 0x1200
	s_mul_i32 s28, s28, s7
	s_addc_u32 s7, s65, 0
	s_add_u32 s8, s64, 0x1300
	s_addc_u32 s9, s65, 0
	s_mov_b32 s29, 1
	s_mov_b64 s[10:11], 0
	s_branch .LBB0_1574

; __device__ __forceinline__ int fresh_tid(int wave) { return wave * 64 + fresh_lane(); }
; __device__ __forceinline__ unsigned xb_ld(unsigned* p)              { return __hip_atomic_load(p, __ATOMIC_RELAXED, __HIP_MEMORY_SCOPE_AGENT); }
; __device__ __forceinline__ unsigned xb_add(unsigned* p, unsigned v) { return __hip_atomic_fetch_add(p, v, __ATOMIC_RELAXED, __HIP_MEMORY_SCOPE_AGENT); }
; __device__ __forceinline__ unsigned xb_xcc_id() { return (unsigned)__builtin_amdgcn_s_getreg((3 << 11) | 20) & 0xFu; }
; #define XB_SPIN(cond, bar) do { unsigned _sp = 0; while (cond) { __builtin_amdgcn_s_sleep(1); \
;     if ((++_sp & 255u) == 0u) { if (xb_ld(&(bar)[XB_TMO])) break; if (_sp > XB_SPIN_CAP) { atomicAdd(&(bar)[XB_TMO], 1u); break; } } } } while (0)
; __device__ __forceinline__ void xcd_barrier(const XcdBarrier& b) {
;     ...
;     if (fresh_tid(b.wave) == 0) {
;         unsigned* bar = b.bar; asm volatile("" : "+s"(bar));
;         __builtin_amdgcn_s_waitcnt(0);
;         const unsigned bx = xb_xcc_id();
;         unsigned nloc = b.st[0], nx = b.st[1];
;         if (nloc == 0u) { xcd_barrier_complete(bar, bx, nloc, nx); b.st[0] = nloc; b.st[1] = nx; }
;         const unsigned old = xb_add(&bar[XB_XSUB(bx)], 1u);
;         const unsigned gen = old / nloc;
;         if (old + 1u == (gen + 1u) * nloc) {
;             __builtin_amdgcn_fence(__ATOMIC_RELEASE, "agent");
;             asm volatile("s_waitcnt vmcnt(0)" ::: "memory");
;             const unsigned og = xb_add(&bar[XB_TOP], 1u);
;             const unsigned tg = og / nx;
;             if (og + 1u == (tg + 1u) * nx) xb_add(&bar[XB_TOPGEN], 1u);
;             else XB_SPIN(xb_ld(&bar[XB_TOPGEN]) == tg, bar);
;             __builtin_amdgcn_fence(__ATOMIC_ACQUIRE, "agent");
;             xb_add(&bar[XB_XGEN(bx)], 1u);
;             asm volatile("s_waitcnt vmcnt(0)" ::: "memory");
;         } else {
;             XB_SPIN(xb_ld(&bar[XB_XGEN(bx)]) == gen, bar);
;             __builtin_amdgcn_fence(__ATOMIC_ACQUIRE, "agent");
;             asm volatile("s_waitcnt vmcnt(0)" ::: "memory");
;         }
.LBB0_1714:
	s_mov_b32 s0, s93
	s_waitcnt vmcnt(0)
	s_waitcnt lgkmcnt(0)
	s_barrier
	s_nop 0
	v_mbcnt_lo_u32_b32 v0, -1, s0
	v_mbcnt_hi_u32_b32 v0, -1, v0
	v_readlane_b32 s0, v254, 17
	s_nop 1
	v_cmp_eq_u32_e32 vcc, s0, v0
	s_and_saveexec_b64 s[38:39], vcc
	s_cbranch_execz .LBB0_1758
	s_bitcmp1_b32 s100, 0
	s_cbranch_scc0 .Lgb9_orig
	v_readlane_b32 s40, v253, 53
	v_readlane_b32 s41, v253, 54
	s_getreg_b32 s0, hwreg(HW_REG_XCC_ID, 0, 4)
	v_mov_b32_e32 v1, 1
	s_and_b32 s0, s0, 15
	s_lshl_b32 s0, s0, 8
	s_addk_i32 s0, 0x1400
	v_mov_b32_e32 v0, s0
	s_waitcnt vmcnt(0) lgkmcnt(0)
	global_atomic_add v2, v0, v1, s[40:41] sc0
	s_waitcnt vmcnt(0)
	v_readfirstlane_b32 s0, v2
	s_lshr_b32 s1, s0, 5
	s_and_b32 s0, s0, 31
	s_add_i32 s1, s1, 1
	s_lshl_b32 s1, s1, 3
	s_cmp_lg_u32 s0, 31
	s_cbranch_scc1 .Lgb9_poll
	buffer_wbl2 sc1
	s_waitcnt vmcnt(0)
	v_add_u32_e32 v0, 0x1000, v0
	global_atomic_add v0, v1, s[40:41]
	v_mov_b32_e32 v0, 0x3400
	global_atomic_add v2, v0, v1, s[40:41] sc0
	s_waitcnt vmcnt(0)
	v_readfirstlane_b32 s0, v2
	s_add_i32 s0, s0, 1
	s_cmp_lg_u32 s0, s1
	s_cbranch_scc1 .Lgb9_poll
	v_mov_b32_e32 v0, 0x3500
	global_atomic_add v0, v1, s[40:41]
	s_branch .Lgb9_done
